# p16_final loops (P17/P18): leftover waits behind the preloaded slot lookups removed: both rows' loads fly together, stores not drained per pair (explicit drain only on the row-1-skipped path)
# speedup vs baseline: 1.0104x; 1.0104x over previous
.LBB0_2155:
	s_cmp_lt_i32 s74, 18
	s_cselect_b64 s[0:1], -1, 0
	s_sub_i32 s30, s30, s33
	s_and_b64 s[8:9], s[0:1], s[6:7]
	s_andn2_b64 vcc, exec, s[8:9]
	s_lshl_b32 s6, s30, 2
	s_cbranch_vccnz .LBB0_2196
	s_cmp_gt_i32 s28, s6
	s_cselect_b64 s[0:1], -1, 0
	s_cmp_lt_i32 s2, s6
	s_cselect_b64 s[10:11], -1, 0
	s_cmp_ge_i32 s2, s6
	s_cselect_b64 s[4:5], -1, 0
	s_and_b64 s[4:5], s[0:1], s[4:5]
	s_mov_b64 s[0:1], -1
	s_and_b64 vcc, exec, s[4:5]
	s_cbranch_vccz .LBB0_2171
	s_sub_i32 s0, s28, s6
	s_lshl_b32 s0, s0, 3
	v_cvt_f32_u32_e32 v1, s0
	v_readlane_b32 s4, v254, 6
	v_readlane_b32 s5, v254, 7
	s_sub_i32 s5, 0, s0
	v_rcp_iflag_f32_e32 v1, v1
	s_sub_i32 s1, s2, s6
	s_lshl_b32 s1, s1, 3
	s_add_i32 s1, s1, s4
	v_mul_f32_e32 v1, 0x4f7ffffe, v1
	v_cvt_u32_f32_e32 v1, v1
	s_add_i32 s4, s0, 0x7fff
	v_readfirstlane_b32 s7, v1
	s_mul_i32 s5, s5, s7
	s_mul_hi_u32 s5, s7, s5
	s_add_i32 s7, s7, s5
	s_mul_hi_u32 s5, s4, s7
	s_mul_i32 s7, s5, s0
	s_sub_i32 s4, s4, s7
	s_add_i32 s12, s5, 1
	s_sub_i32 s7, s4, s0
	s_cmp_ge_u32 s4, s0
	s_cselect_b32 s5, s12, s5
	s_cselect_b32 s4, s7, s4
	s_add_i32 s7, s5, 1
	s_cmp_ge_u32 s4, s0
	s_cselect_b32 s4, s7, s5
	s_add_i32 s4, s4, 1
	s_and_b32 s0, s4, 0x7ffffffe
	s_mul_i32 s12, s0, s1
	s_add_i32 s0, s12, s0
	s_min_i32 s7, s0, 0x8000
	s_cmp_ge_u32 s12, s7
	s_mov_b32 s0, 0
	s_cbranch_scc1 .LBB0_2170
	s_waitcnt vmcnt(0)
	v_lshlrev_b32_e32 v18, 4, v250
	s_waitcnt lgkmcnt(0)
	global_load_dwordx4 v[2:5], v18, s[68:69]
	global_load_dwordx4 v[6:9], v18, s[68:69] offset:1024
	global_load_dwordx4 v[10:13], v18, s[68:69] offset:2048
	global_load_dwordx4 v[14:17], v18, s[68:69] offset:3072
	s_lshl_b32 s24, s31, 14
	s_add_u32 s25, s72, 0x180000
	s_addc_u32 s26, s73, 0
	s_add_u32 s27, s72, 0x140000
	v_lshlrev_b32_e32 v34, 2, v250
	v_mov_b32_e32 v35, 0
	s_addc_u32 s34, s73, 0
	s_lshr_b32 s4, s4, 1
	v_lshl_add_u64 v[26:27], s[72:73], 0, v[34:35]
	s_mov_b64 s[14:15], 0xdd00000
	s_mul_i32 s1, s1, s4
	s_ashr_i32 s13, s12, 31
	v_lshl_add_u64 v[36:37], v[26:27], 0, s[14:15]
	s_lshl_b32 s14, s1, 2
	s_lshl_b64 s[4:5], s[12:13], 11
	s_add_u32 s4, s72, s4
	v_lshlrev_b32_e32 v26, 3, v250
	v_mov_b32_e32 v27, v35
	s_addc_u32 s5, s73, s5
	v_lshl_add_u64 v[26:27], s[4:5], 0, v[26:27]
	s_mov_b64 s[4:5], 0x8c00e00
	v_lshl_add_u64 v[38:39], v[26:27], 0, s[4:5]
	s_lshl_b64 s[4:5], s[12:13], 12
	s_add_u32 s4, s70, s4
	v_mov_b32_e32 v19, v35
	s_addc_u32 s5, s71, s5
	v_or_b32_e32 v20, 0x100, v34
	v_or_b32_e32 v22, 0x200, v34
	v_or_b32_e32 v24, 0x300, v34
	v_lshl_add_u64 v[18:19], s[4:5], 0, v[18:19]
	s_mov_b64 s[16:17], 0x1000
	s_mov_b32 s1, s0
	v_lshl_add_u64 v[40:41], v[18:19], 0, s[16:17]
	s_mov_b32 s36, -1
	v_mov_b64_e32 v[42:43], s[0:1]
	s_add_i32 s13, 0, 0x20100
	v_lshlrev_b32_e32 v1, 2, v34
	v_lshlrev_b32_e32 v34, 2, v20
	v_lshlrev_b32_e32 v66, 2, v22
	v_lshlrev_b32_e32 v67, 2, v24
	v_mov_b32_e32 v68, 0x358637bd
	s_mov_b32 s35, 0x800000
	s_mov_b64 s[18:19], 0x2000
	v_mbcnt_lo_u32_b32 v69, -1, 0
	v_mov_b64_e32 v[44:45], s[0:1]
	v_mov_b32_e32 v18, 0
	v_mov_b32_e32 v19, v35
	v_mov_b32_e32 v20, v35
	v_mov_b32_e32 v21, v35
	v_mov_b32_e32 v22, v35
	v_mov_b32_e32 v23, v35
	v_mov_b32_e32 v24, v35
	v_mov_b32_e32 v25, v35
	v_mov_b32_e32 v26, v35
	v_mov_b32_e32 v27, v35
	v_mov_b32_e32 v28, v35
	v_mov_b32_e32 v29, v35
	v_mov_b32_e32 v30, v35
	v_mov_b32_e32 v31, v35
	v_mov_b32_e32 v32, v35
	v_mov_b32_e32 v33, v35
	v_lshlrev_b32_e32 v248, 2, v250
	s_ashr_i32 s15, s14, 31
	s_lshl_b64 s[98:99], s[14:15], 2
	s_add_u32 s98, s25, s98
	s_addc_u32 s99, s26, s99
	global_load_dword v249, v248, s[98:99]
	s_mov_b32 s100, 0
	s_waitcnt vmcnt(0)
	s_branch .LBB0_2160
.Lp17_drain:
	s_waitcnt vmcnt(0)
	s_branch .LBB0_2164
.LBB0_2159:
	s_add_i32 s12, s12, 2
	s_add_i32 s14, s14, 4
	s_add_i32 s100, s100, 4
	v_lshl_add_u64 v[38:39], v[38:39], 0, s[16:17]
	s_cmp_lt_i32 s12, s7
	v_lshl_add_u64 v[40:41], v[40:41], 0, s[18:19]
	s_cbranch_scc0 .LBB0_2170
.LBB0_2160:
	s_ashr_i32 s15, s14, 31
	s_lshl_b64 s[0:1], s[14:15], 2
	s_add_u32 s4, s25, s0
	s_addc_u32 s5, s26, s1
	v_readlane_b32 s98, v249, s100
	s_add_i32 s4, s14, 1
	s_ashr_i32 s5, s4, 31
	s_lshl_b64 s[20:21], s[4:5], 2
	s_add_u32 s4, s25, s20
	s_addc_u32 s5, s26, s21
	s_add_i32 s101, s100, 1
	v_readlane_b32 s99, v249, s101
	s_nop 1
	v_mov_b32_e32 v62, s98
	v_mov_b32_e32 v63, s99
	v_ashrrev_i32_e32 v64, 15, v62
	v_lshlrev_b32_e32 v64, 2, v64
	v_add_u32_e32 v64, s13, v64
	ds_read_b32 v64, v64
	v_and_b32_e32 v62, 0x7fff, v62
	v_ashrrev_i32_e32 v65, 15, v63
	v_lshlrev_b32_e32 v65, 2, v65
	v_add_u32_e32 v65, s13, v65
	ds_read_b32 v65, v65
	s_waitcnt lgkmcnt(1)
	v_lshlrev_b32_e32 v64, 8, v64
	v_add_u32_e32 v64, v64, v62
	v_and_b32_e32 v63, 0x7fff, v63
	s_waitcnt lgkmcnt(0)
	v_lshlrev_b32_e32 v62, 8, v65
	v_add_u32_e32 v62, v62, v63
	v_max_i32_e32 v63, v64, v62
	v_cmp_gt_i32_e64 s[4:5], s24, v63
	s_and_b64 vcc, exec, s[4:5]
	s_cbranch_vccz .LBB0_2162
	s_add_u32 s0, s27, s0
	v_ashrrev_i32_e32 v65, 31, v64
	s_addc_u32 s1, s34, s1
	v_lshlrev_b64 v[52:53], 10, v[64:65]
	v_ashrrev_i32_e32 v63, 31, v62
	s_add_u32 s20, s27, s20
	v_lshl_add_u64 v[64:65], v[36:37], 0, v[52:53]
	v_lshlrev_b64 v[52:53], 10, v[62:63]
	s_addc_u32 s21, s34, s21
	global_load_dword v42, v35, s[0:1]
	global_load_dword v44, v35, s[20:21]
	v_lshl_add_u64 v[62:63], v[36:37], 0, v[52:53]
	global_load_dwordx2 v[52:53], v[38:39], off offset:-3584
	global_load_dwordx2 v[56:57], v[38:39], off offset:-3072
	global_load_dwordx2 v[58:59], v[38:39], off offset:-2560
	global_load_dwordx2 v[60:61], v[38:39], off offset:-2048
	global_load_dword v73, v[64:65], off
	global_load_dword v82, v[62:63], off
	global_load_dword v75, v[64:65], off offset:256
	global_load_dword v83, v[62:63], off offset:256
	global_load_dword v76, v[64:65], off offset:512
	global_load_dword v84, v[62:63], off offset:512
	global_load_dword v85, v[62:63], off offset:768
	global_load_dword v78, v[64:65], off offset:768
	s_waitcnt vmcnt(13)
	v_mul_f32_e32 v42, 0x3d800000, v42
	s_waitcnt vmcnt(12)
	v_mul_f32_e32 v44, 0x3d800000, v44
.LBB0_2162:
	s_add_i32 s0, s14, 2
	s_ashr_i32 s1, s0, 31
	s_lshl_b64 s[20:21], s[0:1], 2
	s_add_u32 s0, s25, s20
	s_addc_u32 s1, s26, s21
	s_add_i32 s101, s100, 2
	v_readlane_b32 s98, v249, s101
	s_add_i32 s0, s14, 3
	s_ashr_i32 s1, s0, 31
	s_lshl_b64 s[22:23], s[0:1], 2
	s_add_u32 s0, s25, s22
	s_addc_u32 s1, s26, s23
	s_add_i32 s101, s100, 3
	v_readlane_b32 s99, v249, s101
	s_nop 1
	v_mov_b32_e32 v62, s98
	v_mov_b32_e32 v63, s99
	v_ashrrev_i32_e32 v64, 15, v62
	v_lshlrev_b32_e32 v64, 2, v64
	v_add_u32_e32 v64, s13, v64
	ds_read_b32 v64, v64
	v_and_b32_e32 v62, 0x7fff, v62
	v_ashrrev_i32_e32 v65, 15, v63
	v_lshlrev_b32_e32 v65, 2, v65
	v_add_u32_e32 v65, s13, v65
	ds_read_b32 v65, v65
	s_waitcnt lgkmcnt(1)
	v_lshlrev_b32_e32 v64, 8, v64
	v_add_u32_e32 v64, v64, v62
	v_and_b32_e32 v63, 0x7fff, v63
	s_waitcnt lgkmcnt(0)
	v_lshlrev_b32_e32 v62, 8, v65
	v_add_u32_e32 v62, v62, v63
	v_max_i32_e32 v63, v64, v62
	v_cmp_le_i32_e32 vcc, s24, v63
	v_cmp_gt_i32_e64 s[0:1], s24, v63
	s_cbranch_vccnz .Lp17_drain
	s_add_u32 s20, s27, s20
	v_ashrrev_i32_e32 v65, 31, v64
	s_addc_u32 s21, s34, s21
	v_lshlrev_b64 v[46:47], 10, v[64:65]
	v_ashrrev_i32_e32 v63, 31, v62
	s_add_u32 s22, s27, s22
	v_lshl_add_u64 v[64:65], v[36:37], 0, v[46:47]
	v_lshlrev_b64 v[46:47], 10, v[62:63]
	s_addc_u32 s23, s34, s23
	global_load_dword v43, v35, s[20:21]
	global_load_dword v45, v35, s[22:23]
	v_lshl_add_u64 v[62:63], v[36:37], 0, v[46:47]
	global_load_dwordx2 v[46:47], v[38:39], off offset:-1536
	global_load_dwordx2 v[48:49], v[38:39], off offset:-1024
	global_load_dwordx2 v[50:51], v[38:39], off offset:-512
	global_load_dwordx2 v[54:55], v[38:39], off
	global_load_dword v70, v[64:65], off
	global_load_dword v77, v[62:63], off
	global_load_dword v71, v[64:65], off offset:256
	global_load_dword v79, v[62:63], off offset:256
	global_load_dword v72, v[64:65], off offset:512
	global_load_dword v80, v[62:63], off offset:512
	global_load_dword v81, v[62:63], off offset:768
	global_load_dword v74, v[64:65], off offset:768
	s_waitcnt vmcnt(13)
	v_mul_f32_e32 v43, 0x3d800000, v43
	s_waitcnt vmcnt(12)
	v_mul_f32_e32 v45, 0x3d800000, v45

.LBB0_2296:
	s_cmp_lt_i32 s74, 19
	s_cselect_b64 s[0:1], -1, 0
	s_and_b64 s[0:1], s[0:1], s[2:3]
	s_andn2_b64 vcc, exec, s[0:1]
	s_cbranch_vccnz .LBB0_2310
	v_readlane_b32 s2, v254, 9
	s_abs_i32 s0, s2
	v_cvt_f32_u32_e32 v0, s0
	s_sub_i32 s3, 0, s0
	s_add_i32 s1, s2, 0x7fff
	s_xor_b32 s2, s1, s2
	v_rcp_iflag_f32_e32 v0, v0
	s_abs_i32 s1, s1
	s_ashr_i32 s2, s2, 31
	v_mul_f32_e32 v0, 0x4f7ffffe, v0
	v_cvt_u32_f32_e32 v0, v0
	s_nop 0
	v_readfirstlane_b32 s4, v0
	s_mul_i32 s3, s3, s4
	s_mul_hi_u32 s3, s4, s3
	s_add_i32 s4, s4, s3
	s_mul_hi_u32 s3, s1, s4
	s_mul_i32 s4, s3, s0
	s_sub_i32 s1, s1, s4
	s_add_i32 s5, s3, 1
	s_sub_i32 s4, s1, s0
	s_cmp_ge_u32 s1, s0
	s_cselect_b32 s3, s5, s3
	s_cselect_b32 s1, s4, s1
	s_add_i32 s4, s3, 1
	s_cmp_ge_u32 s1, s0
	s_cselect_b32 s0, s4, s3
	s_xor_b32 s0, s0, s2
	s_sub_i32 s1, s0, s2
	s_add_i32 s1, s1, 1
	s_and_b32 s0, s1, -2
	s_mul_i32 s2, s0, s97
	s_add_i32 s0, s2, s0
	s_min_i32 s18, s0, 0x8000
	s_cmp_ge_i32 s2, s18
	s_mov_b32 s0, 0
	s_cbranch_scc1 .LBB0_2310
	s_waitcnt vmcnt(0) lgkmcnt(0)
	v_lshlrev_b32_e32 v16, 4, v250
	global_load_dwordx4 v[0:3], v16, s[68:69]
	global_load_dwordx4 v[4:7], v16, s[68:69] offset:1024
	global_load_dwordx4 v[8:11], v16, s[68:69] offset:2048
	global_load_dwordx4 v[12:15], v16, s[68:69] offset:3072
	s_lshl_b32 s19, s31, 14
	s_add_u32 s20, s72, 0x180000
	s_addc_u32 s21, s73, 0
	s_add_u32 s22, s72, 0x140000
	s_addc_u32 s23, s73, 0
	s_cmp_le_i32 s28, s6
	v_lshlrev_b32_e32 v32, 2, v250
	v_mov_b32_e32 v33, 0
	s_cselect_b64 s[4:5], -1, 0
	s_lshr_b32 s1, s1, 1
	v_lshl_add_u64 v[24:25], s[72:73], 0, v[32:33]
	s_mov_b64 s[6:7], 0xdd00000
	s_mul_i32 s1, s1, s97
	s_ashr_i32 s3, s2, 31
	v_lshl_add_u64 v[34:35], v[24:25], 0, s[6:7]
	s_lshl_b32 s6, s1, 2
	s_lshl_b64 s[8:9], s[2:3], 11
	s_add_u32 s8, s72, s8
	v_lshlrev_b32_e32 v24, 3, v250
	v_mov_b32_e32 v25, v33
	s_addc_u32 s9, s73, s9
	v_lshl_add_u64 v[24:25], s[8:9], 0, v[24:25]
	s_mov_b64 s[8:9], 0x8c00e00
	v_lshl_add_u64 v[36:37], v[24:25], 0, s[8:9]
	s_lshl_b64 s[8:9], s[2:3], 12
	s_add_u32 s8, s70, s8
	v_mov_b32_e32 v17, v33
	s_addc_u32 s9, s71, s9
	v_lshl_add_u64 v[16:17], s[8:9], 0, v[16:17]
	s_mov_b64 s[8:9], 0x1000
	v_or_b32_e32 v18, 0x100, v32
	v_or_b32_e32 v20, 0x200, v32
	v_or_b32_e32 v22, 0x300, v32
	v_lshl_add_u64 v[38:39], v[16:17], 0, s[8:9]
	s_mov_b32 s1, s0
	v_mbcnt_lo_u32_b32 v16, -1, 0
	s_mov_b32 s25, -1
	v_mov_b64_e32 v[40:41], s[0:1]
	s_add_i32 s3, 0, 0x20100
	v_lshlrev_b32_e32 v32, 2, v32
	v_lshlrev_b32_e32 v64, 2, v18
	v_lshlrev_b32_e32 v65, 2, v20
	v_lshlrev_b32_e32 v66, 2, v22
	v_mov_b32_e32 v67, 0x358637bd
	s_mov_b32 s24, 0x800000
	s_mov_b64 s[10:11], 0x2000
	v_mbcnt_hi_u32_b32 v68, -1, v16
	v_mov_b64_e32 v[42:43], s[0:1]
	v_mov_b32_e32 v16, 0
	v_mov_b32_e32 v17, v33
	v_mov_b32_e32 v18, v33
	v_mov_b32_e32 v19, v33
	v_mov_b32_e32 v20, v33
	v_mov_b32_e32 v21, v33
	v_mov_b32_e32 v22, v33
	v_mov_b32_e32 v23, v33
	v_mov_b32_e32 v24, v33
	v_mov_b32_e32 v25, v33
	v_mov_b32_e32 v26, v33
	v_mov_b32_e32 v27, v33
	v_mov_b32_e32 v28, v33
	v_mov_b32_e32 v29, v33
	v_mov_b32_e32 v30, v33
	v_mov_b32_e32 v31, v33
	v_lshlrev_b32_e32 v248, 2, v250
	s_ashr_i32 s7, s6, 31
	s_lshl_b64 s[98:99], s[6:7], 2
	s_add_u32 s98, s20, s98
	s_addc_u32 s99, s21, s99
	global_load_dword v249, v248, s[98:99]
	s_mov_b32 s100, 0
	s_waitcnt vmcnt(0)
	s_branch .LBB0_2300
.Lp18_drain:
	s_waitcnt vmcnt(0)
	s_branch .LBB0_2304
.LBB0_2299:
	s_add_i32 s2, s2, 2
	s_add_i32 s6, s6, 4
	s_add_i32 s100, s100, 4
	v_lshl_add_u64 v[36:37], v[36:37], 0, s[8:9]
	s_cmp_lt_i32 s2, s18
	v_lshl_add_u64 v[38:39], v[38:39], 0, s[10:11]
	s_cbranch_scc0 .LBB0_2310
.LBB0_2300:
	s_ashr_i32 s7, s6, 31
	s_lshl_b64 s[0:1], s[6:7], 2
	s_add_u32 s12, s20, s0
	s_addc_u32 s13, s21, s1
	v_readlane_b32 s98, v249, s100
	s_add_i32 s12, s6, 1
	s_ashr_i32 s13, s12, 31
	s_lshl_b64 s[14:15], s[12:13], 2
	s_add_u32 s12, s20, s14
	s_addc_u32 s13, s21, s15
	s_add_i32 s101, s100, 1
	v_readlane_b32 s99, v249, s101
	s_nop 1
	v_mov_b32_e32 v60, s98
	v_mov_b32_e32 v61, s99
	v_ashrrev_i32_e32 v62, 15, v60
	v_lshlrev_b32_e32 v62, 2, v62
	v_add_u32_e32 v62, s3, v62
	ds_read_b32 v62, v62
	v_and_b32_e32 v60, 0x7fff, v60
	v_ashrrev_i32_e32 v63, 15, v61
	v_lshlrev_b32_e32 v63, 2, v63
	v_add_u32_e32 v63, s3, v63
	ds_read_b32 v63, v63
	s_waitcnt lgkmcnt(1)
	v_lshlrev_b32_e32 v62, 8, v62
	v_add_u32_e32 v62, v62, v60
	v_and_b32_e32 v61, 0x7fff, v61
	s_waitcnt lgkmcnt(0)
	v_lshlrev_b32_e32 v60, 8, v63
	v_add_u32_e32 v60, v60, v61
	v_max_i32_e32 v61, v62, v60
	v_cmp_le_i32_e32 vcc, s19, v61
	s_or_b64 s[12:13], s[4:5], vcc
	s_and_b64 vcc, exec, s[12:13]
	s_cbranch_vccz .LBB0_2302
	s_add_u32 s0, s22, s0
	v_ashrrev_i32_e32 v63, 31, v62
	s_addc_u32 s1, s23, s1
	v_lshlrev_b64 v[50:51], 10, v[62:63]
	v_ashrrev_i32_e32 v61, 31, v60
	s_add_u32 s14, s22, s14
	v_lshl_add_u64 v[62:63], v[34:35], 0, v[50:51]
	v_lshlrev_b64 v[50:51], 10, v[60:61]
	s_addc_u32 s15, s23, s15
	global_load_dword v40, v33, s[0:1]
	global_load_dword v42, v33, s[14:15]
	v_lshl_add_u64 v[60:61], v[34:35], 0, v[50:51]
	global_load_dwordx2 v[50:51], v[36:37], off offset:-3584
	global_load_dwordx2 v[54:55], v[36:37], off offset:-3072
	global_load_dwordx2 v[56:57], v[36:37], off offset:-2560
	global_load_dwordx2 v[58:59], v[36:37], off offset:-2048
	global_load_dword v72, v[62:63], off
	global_load_dword v81, v[60:61], off
	global_load_dword v74, v[62:63], off offset:256
	global_load_dword v82, v[60:61], off offset:256
	global_load_dword v75, v[62:63], off offset:512
	global_load_dword v83, v[60:61], off offset:512
	global_load_dword v84, v[60:61], off offset:768
	global_load_dword v77, v[62:63], off offset:768
	s_waitcnt vmcnt(13)
	v_mul_f32_e32 v40, 0x3d800000, v40
	s_waitcnt vmcnt(12)
	v_mul_f32_e32 v42, 0x3d800000, v42
.LBB0_2302:
	s_add_i32 s0, s6, 2
	s_ashr_i32 s1, s0, 31
	s_lshl_b64 s[14:15], s[0:1], 2
	s_add_u32 s0, s20, s14
	s_addc_u32 s1, s21, s15
	s_add_i32 s101, s100, 2
	v_readlane_b32 s98, v249, s101
	s_add_i32 s0, s6, 3
	s_ashr_i32 s1, s0, 31
	s_lshl_b64 s[16:17], s[0:1], 2
	s_add_u32 s0, s20, s16
	s_addc_u32 s1, s21, s17
	s_add_i32 s101, s100, 3
	v_readlane_b32 s99, v249, s101
	s_nop 1
	v_mov_b32_e32 v60, s98
	v_mov_b32_e32 v61, s99
	v_ashrrev_i32_e32 v62, 15, v60
	v_lshlrev_b32_e32 v62, 2, v62
	v_add_u32_e32 v62, s3, v62
	ds_read_b32 v62, v62
	v_and_b32_e32 v60, 0x7fff, v60
	v_ashrrev_i32_e32 v63, 15, v61
	v_lshlrev_b32_e32 v63, 2, v63
	v_add_u32_e32 v63, s3, v63
	ds_read_b32 v63, v63
	s_waitcnt lgkmcnt(1)
	v_lshlrev_b32_e32 v62, 8, v62
	v_and_b32_e32 v61, 0x7fff, v61
	v_add_u32_e32 v62, v62, v60
	s_waitcnt lgkmcnt(0)
	v_lshlrev_b32_e32 v60, 8, v63
	v_add_u32_e32 v60, v60, v61
	v_max_i32_e32 v61, v62, v60
	v_cmp_le_i32_e32 vcc, s19, v61
	s_or_b64 s[26:27], s[4:5], vcc
	v_cndmask_b32_e64 v61, 0, 1, s[26:27]
	v_cmp_ne_u32_e64 s[0:1], 1, v61
	s_andn2_b64 vcc, exec, s[26:27]
	s_cbranch_vccnz .Lp18_drain
	s_add_u32 s14, s22, s14
	v_ashrrev_i32_e32 v63, 31, v62
	s_addc_u32 s15, s23, s15
	v_lshlrev_b64 v[44:45], 10, v[62:63]
	v_ashrrev_i32_e32 v61, 31, v60
	s_add_u32 s16, s22, s16
	v_lshl_add_u64 v[62:63], v[34:35], 0, v[44:45]
	v_lshlrev_b64 v[44:45], 10, v[60:61]
	s_addc_u32 s17, s23, s17
	global_load_dword v41, v33, s[14:15]
	global_load_dword v43, v33, s[16:17]
	v_lshl_add_u64 v[60:61], v[34:35], 0, v[44:45]
	global_load_dwordx2 v[44:45], v[36:37], off offset:-1536
	global_load_dwordx2 v[46:47], v[36:37], off offset:-1024
	global_load_dwordx2 v[48:49], v[36:37], off offset:-512
	global_load_dwordx2 v[52:53], v[36:37], off
	global_load_dword v69, v[62:63], off
	global_load_dword v76, v[60:61], off
	global_load_dword v70, v[62:63], off offset:256
	global_load_dword v78, v[60:61], off offset:256
	global_load_dword v71, v[62:63], off offset:512
	global_load_dword v79, v[60:61], off offset:512
	global_load_dword v80, v[60:61], off offset:768
	global_load_dword v73, v[62:63], off offset:768
	s_waitcnt vmcnt(13)
	v_mul_f32_e32 v41, 0x3d800000, v41
	s_waitcnt vmcnt(12)
	v_mul_f32_e32 v43, 0x3d800000, v43
